# speedup vs baseline: 1.0380x; 1.0380x over previous
_Z11prep_kernelPKfS0_S0_S0_S0_S0_S0_S0_S0_PKiPDv8_DF16bS4_PfS5_S5_PiPt:
	s_load_dwordx4 s[16:19], s[0:1], 0x0
	s_load_dwordx4 s[20:23], s[0:1], 0x10
	s_load_dwordx4 s[24:27], s[0:1], 0x20
	s_load_dwordx4 s[28:31], s[0:1], 0x30
	s_load_dwordx4 s[32:35], s[0:1], 0x40
	s_load_dwordx2 s[36:37], s[0:1], 0x80
	v_and_b32_e32 v126, 63, v0
	v_lshrrev_b32_e32 v128, 6, v0
	v_and_b32_e32 v1, 15, v0
	v_bfe_u32 v24, v0, 4, 2
	v_lshl_or_b32 v107, v128, 4, v1
	v_lshlrev_b32_e32 v106, 2, v107
	v_lshlrev_b32_e32 v127, 2, v0
	v_lshlrev_b32_e32 v25, 1, v107
	v_and_b32_e32 v26, 48, v0
	v_mul_u32_u24_e32 v27, 0x440, v24
	v_lshlrev_b32_e32 v120, 4, v0
	v_lshrrev_b32_e32 v58, 5, v0
	v_mul_u32_u24_e32 v58, 0x110, v58
	v_and_b32_e32 v125, 31, v0
	v_lshl_add_u32 v58, v125, 3, v58
	v_add_u32_e32 v124, 0x1b400, v58
	v_mul_u32_u24_e32 v52, 0x110, v1
	v_add_u32_e32 v52, v52, v26
	v_add_u32_e32 v53, 0x1b400, v52
	v_add_u32_e32 v54, 0x1c500, v52
	v_add_u32_e32 v55, v27, v25
	v_add_u32_e32 v55, 0x1c500, v55
	v_mul_u32_u24_e32 v56, 0x110, v107
	v_add_u32_e32 v56, v56, v26
	v_add_u32_e32 v57, 0x8800, v56
	s_lshl_b32 s12, s2, 4
	s_add_i32 s3, s12, 0xfffff800
	s_cmpk_gt_i32 s2, 0x7f
	s_cselect_b64 s[6:7], -1, 0
	s_mov_b32 s48, 0
	s_mov_b32 s49, -1
	v_lshl_or_b32 v123, s2, 3, v128
	v_lshlrev_b32_e32 v123, 12, v123
	v_lshl_add_u32 v123, v126, 4, v123
	s_waitcnt lgkmcnt(0)
	s_cmpk_lt_i32 s2, 0x80
	s_cselect_b32 s38, s16, s18
	s_cselect_b32 s39, s17, s19
	s_cselect_b32 s40, s20, s24
	s_cselect_b32 s41, s21, s25
	s_cselect_b32 s13, s12, s3
	s_cselect_b32 s44, 0x3db504f3, 1.0
	s_lshl_b32 s13, s13, 9
	s_add_u32 s38, s38, s13
	s_addc_u32 s39, s39, 0
	global_load_dwordx4 v[2:5], v120, s[38:39] nt
	s_and_b32 s13, s2, 7
	s_lshl_b32 s14, s13, 13
	v_add_u32_e32 v125, s14, v120
	global_load_dwordx4 v[80:83], v125, s[40:41]
	s_add_i32 s13, s2, 1
	s_and_b32 s13, s13, 7
	s_lshl_b32 s14, s13, 13
	v_add_u32_e32 v125, s14, v120
	global_load_dwordx4 v[84:87], v125, s[40:41]
	s_add_i32 s13, s2, 2
	s_and_b32 s13, s13, 7
	s_lshl_b32 s14, s13, 13
	v_add_u32_e32 v125, s14, v120
	global_load_dwordx4 v[88:91], v125, s[40:41]
	s_add_i32 s13, s2, 3
	s_and_b32 s13, s13, 7
	s_lshl_b32 s14, s13, 13
	v_add_u32_e32 v125, s14, v120
	global_load_dwordx4 v[92:95], v125, s[40:41]
	s_add_i32 s13, s2, 4
	s_and_b32 s13, s13, 7
	s_lshl_b32 s14, s13, 13
	v_add_u32_e32 v125, s14, v120
	global_load_dwordx4 v[96:99], v125, s[40:41]
	s_add_i32 s13, s2, 5
	s_and_b32 s13, s13, 7
	s_lshl_b32 s14, s13, 13
	v_add_u32_e32 v125, s14, v120
	global_load_dwordx4 v[100:103], v125, s[40:41]
	s_add_i32 s13, s2, 6
	s_and_b32 s13, s13, 7
	s_lshl_b32 s14, s13, 13
	v_add_u32_e32 v125, s14, v120
	global_load_dwordx4 v[108:111], v125, s[40:41]
	s_add_i32 s13, s2, 7
	s_and_b32 s13, s13, 7
	s_lshl_b32 s14, s13, 13
	v_add_u32_e32 v125, s14, v120
	global_load_dwordx4 v[112:115], v125, s[40:41]
	global_load_dword v129, v106, s[32:33]
	global_load_dword v130, v106, s[30:31]
	s_and_b64 vcc, exec, s[6:7]
	s_cbranch_vccz .Lp_q
	v_cmp_gt_u32_e32 vcc, 32, v126
	v_mov_b32_e32 v198, 0x3db504f3
	v_mov_b32_e32 v125, s22
	v_mov_b32_e32 v104, s26
	v_cndmask_b32_e32 v198, 1.0, v198, vcc
	v_cndmask_b32_e32 v104, v104, v125, vcc
	v_mov_b32_e32 v125, s23
	v_mov_b32_e32 v105, s27
	v_cndmask_b32_e32 v105, v105, v125, vcc
	v_and_b32_e32 v196, 31, v126
	v_lshlrev_b32_e32 v196, 4, v196
	v_mov_b32_e32 v197, 0
	v_lshl_add_u64 v[104:105], v[104:105], 0, v[196:197]
	global_load_dwordx4 v[116:119], v[104:105], off
	v_lshlrev_b32_e32 v121, 14, v128
	v_lshl_add_u32 v121, v126, 4, v121
	s_and_b32 s13, s2, 15
	s_lshl_b32 s14, s13, 10
	s_add_u32 s46, s28, s14
	s_addc_u32 s47, s29, 0
	global_load_dwordx4 v[132:135], v121, s[46:47]
	s_add_i32 s13, s2, 1
	s_and_b32 s13, s13, 15
	s_lshl_b32 s14, s13, 10
	s_add_u32 s46, s28, s14
	s_addc_u32 s47, s29, 0
	global_load_dwordx4 v[136:139], v121, s[46:47]
	s_add_i32 s13, s2, 2
	s_and_b32 s13, s13, 15
	s_lshl_b32 s14, s13, 10
	s_add_u32 s46, s28, s14
	s_addc_u32 s47, s29, 0
	global_load_dwordx4 v[140:143], v121, s[46:47]
	s_add_i32 s13, s2, 3
	s_and_b32 s13, s13, 15
	s_lshl_b32 s14, s13, 10
	s_add_u32 s46, s28, s14
	s_addc_u32 s47, s29, 0
	global_load_dwordx4 v[144:147], v121, s[46:47]
	s_add_i32 s13, s2, 4
	s_and_b32 s13, s13, 15
	s_lshl_b32 s14, s13, 10
	s_add_u32 s46, s28, s14
	s_addc_u32 s47, s29, 0
	global_load_dwordx4 v[148:151], v121, s[46:47]
	s_add_i32 s13, s2, 5
	s_and_b32 s13, s13, 15
	s_lshl_b32 s14, s13, 10
	s_add_u32 s46, s28, s14
	s_addc_u32 s47, s29, 0
	global_load_dwordx4 v[152:155], v121, s[46:47]
	s_add_i32 s13, s2, 6
	s_and_b32 s13, s13, 15
	s_lshl_b32 s14, s13, 10
	s_add_u32 s46, s28, s14
	s_addc_u32 s47, s29, 0
	global_load_dwordx4 v[156:159], v121, s[46:47]
	s_add_i32 s13, s2, 7
	s_and_b32 s13, s13, 15
	s_lshl_b32 s14, s13, 10
	s_add_u32 s46, s28, s14
	s_addc_u32 s47, s29, 0
	global_load_dwordx4 v[160:163], v121, s[46:47]
	s_add_i32 s13, s2, 8
	s_and_b32 s13, s13, 15
	s_lshl_b32 s14, s13, 10
	s_add_u32 s46, s28, s14
	s_addc_u32 s47, s29, 0
	global_load_dwordx4 v[164:167], v121, s[46:47]
	s_add_i32 s13, s2, 9
	s_and_b32 s13, s13, 15
	s_lshl_b32 s14, s13, 10
	s_add_u32 s46, s28, s14
	s_addc_u32 s47, s29, 0
	global_load_dwordx4 v[168:171], v121, s[46:47]
	s_add_i32 s13, s2, 10
	s_and_b32 s13, s13, 15
	s_lshl_b32 s14, s13, 10
	s_add_u32 s46, s28, s14
	s_addc_u32 s47, s29, 0
	global_load_dwordx4 v[172:175], v121, s[46:47]
	s_add_i32 s13, s2, 11
	s_and_b32 s13, s13, 15
	s_lshl_b32 s14, s13, 10
	s_add_u32 s46, s28, s14
	s_addc_u32 s47, s29, 0
	global_load_dwordx4 v[176:179], v121, s[46:47]
	s_add_i32 s13, s2, 12
	s_and_b32 s13, s13, 15
	s_lshl_b32 s14, s13, 10
	s_add_u32 s46, s28, s14
	s_addc_u32 s47, s29, 0
	global_load_dwordx4 v[180:183], v121, s[46:47]
	s_add_i32 s13, s2, 13
	s_and_b32 s13, s13, 15
	s_lshl_b32 s14, s13, 10
	s_add_u32 s46, s28, s14
	s_addc_u32 s47, s29, 0
	global_load_dwordx4 v[184:187], v121, s[46:47]
	s_add_i32 s13, s2, 14
	s_and_b32 s13, s13, 15
	s_lshl_b32 s14, s13, 10
	s_add_u32 s46, s28, s14
	s_addc_u32 s47, s29, 0
	global_load_dwordx4 v[188:191], v121, s[46:47]
	s_add_i32 s13, s2, 15
	s_and_b32 s13, s13, 15
	s_lshl_b32 s14, s13, 10
	s_add_u32 s46, s28, s14
	s_addc_u32 s47, s29, 0
	global_load_dwordx4 v[192:195], v121, s[46:47]
	v_mul_u32_u24_e32 v59, 0x1040, v128
	v_lshl_add_u32 v59, v126, 2, v59
	v_add_u32_e32 v59, 0x11000, v59
	v_mul_u32_u24_e32 v76, 0x1100, v128
	v_lshl_add_u32 v76, v126, 3, v76
	v_add_u32_e32 v76, 0x8700, v76
	v_lshrrev_b32_e32 v77, 2, v126
	v_mul_u32_u24_e32 v77, 0x104, v77
	v_mul_u32_u24_e32 v125, 0x1040, v128
	v_add_u32_e32 v77, v77, v125
	v_and_b32_e32 v125, 3, v126
	v_lshl_add_u32 v77, v125, 6, v77
	v_add_u32_e32 v77, 0x11000, v77
	s_waitcnt vmcnt(27)
	v_cvt_pk_bf16_f32 v12, v2, v3
	v_cvt_pk_bf16_f32 v13, v4, v5
	ds_write_b64 v124, v[12:13]
	s_waitcnt vmcnt(26)
	v_cvt_pk_bf16_f32 v6, v80, v81
	v_cvt_pk_bf16_f32 v7, v82, v83
	s_and_b32 s13, s2, 7
	s_mul_i32 s14, s13, 0x1100
	v_add_u32_e32 v125, s14, v58
	ds_write_b64 v125, v[6:7]
	s_waitcnt vmcnt(25)
	v_cvt_pk_bf16_f32 v8, v84, v85
	v_cvt_pk_bf16_f32 v9, v86, v87
	s_add_i32 s13, s2, 1
	s_and_b32 s13, s13, 7
	s_mul_i32 s14, s13, 0x1100
	v_add_u32_e32 v10, s14, v58
	ds_write_b64 v10, v[8:9]
	s_waitcnt vmcnt(24)
	v_cvt_pk_bf16_f32 v6, v88, v89
	v_cvt_pk_bf16_f32 v7, v90, v91
	s_add_i32 s13, s2, 2
	s_and_b32 s13, s13, 7
	s_mul_i32 s14, s13, 0x1100
	v_add_u32_e32 v125, s14, v58
	ds_write_b64 v125, v[6:7]
	s_waitcnt vmcnt(23)
	v_cvt_pk_bf16_f32 v8, v92, v93
	v_cvt_pk_bf16_f32 v9, v94, v95
	s_add_i32 s13, s2, 3
	s_and_b32 s13, s13, 7
	s_mul_i32 s14, s13, 0x1100
	v_add_u32_e32 v10, s14, v58
	ds_write_b64 v10, v[8:9]
	s_waitcnt vmcnt(22)
	v_cvt_pk_bf16_f32 v6, v96, v97
	v_cvt_pk_bf16_f32 v7, v98, v99
	s_add_i32 s13, s2, 4
	s_and_b32 s13, s13, 7
	s_mul_i32 s14, s13, 0x1100
	v_add_u32_e32 v125, s14, v58
	ds_write_b64 v125, v[6:7]
	s_waitcnt vmcnt(21)
	v_cvt_pk_bf16_f32 v8, v100, v101
	v_cvt_pk_bf16_f32 v9, v102, v103
	s_add_i32 s13, s2, 5
	s_and_b32 s13, s13, 7
	s_mul_i32 s14, s13, 0x1100
	v_add_u32_e32 v10, s14, v58
	ds_write_b64 v10, v[8:9]
	s_waitcnt vmcnt(20)
	v_cvt_pk_bf16_f32 v6, v108, v109
	v_cvt_pk_bf16_f32 v7, v110, v111
	s_add_i32 s13, s2, 6
	s_and_b32 s13, s13, 7
	s_mul_i32 s14, s13, 0x1100
	v_add_u32_e32 v125, s14, v58
	ds_write_b64 v125, v[6:7]
	s_waitcnt vmcnt(19)
	v_cvt_pk_bf16_f32 v8, v112, v113
	v_cvt_pk_bf16_f32 v9, v114, v115
	s_add_i32 s13, s2, 7
	s_and_b32 s13, s13, 7
	s_mul_i32 s14, s13, 0x1100
	v_add_u32_e32 v10, s14, v58
	ds_write_b64 v10, v[8:9]
	s_waitcnt vmcnt(16)
	v_pk_mul_f32 v[116:117], v[198:199], v[116:117] op_sel_hi:[0,1]
	v_pk_mul_f32 v[118:119], v[198:199], v[118:119] op_sel_hi:[0,1]
	s_waitcnt vmcnt(15)
	v_mul_f32_e32 v6, v117, v133
	v_mul_f32_e32 v7, v119, v135
	v_fmac_f32_e32 v6, v116, v132
	v_fmac_f32_e32 v7, v118, v134
	s_and_b32 s13, s2, 15
	s_mul_i32 s14, s13, 0x104
	s_mul_i32 s15, s13, 0x110
	v_add_f32_e32 v6, v6, v7
	v_add_u32_e32 v125, s14, v59
	ds_write_b32 v125, v6
	v_cvt_pk_bf16_f32 v8, v132, v133
	v_cvt_pk_bf16_f32 v9, v134, v135
	v_add_u32_e32 v10, s15, v76
	s_mov_b64 exec, s[48:49]
	ds_write_b64 v10, v[8:9]
	s_mov_b64 exec, -1
	s_waitcnt vmcnt(14)
	v_mul_f32_e32 v11, v117, v137
	v_mul_f32_e32 v15, v119, v139
	v_fmac_f32_e32 v11, v116, v136
	v_fmac_f32_e32 v15, v118, v138
	s_add_i32 s13, s2, 1
	s_and_b32 s13, s13, 15
	s_mul_i32 s14, s13, 0x104
	s_mul_i32 s15, s13, 0x110
	v_add_f32_e32 v11, v11, v15
	v_add_u32_e32 v16, s14, v59
	ds_write_b32 v16, v11
	v_cvt_pk_bf16_f32 v12, v136, v137
	v_cvt_pk_bf16_f32 v13, v138, v139
	v_add_u32_e32 v14, s15, v76
	s_mov_b64 exec, s[48:49]
	ds_write_b64 v14, v[12:13]
	s_mov_b64 exec, -1
	s_waitcnt vmcnt(13)
	v_mul_f32_e32 v6, v117, v141
	v_mul_f32_e32 v7, v119, v143
	v_fmac_f32_e32 v6, v116, v140
	v_fmac_f32_e32 v7, v118, v142
	s_add_i32 s13, s2, 2
	s_and_b32 s13, s13, 15
	s_mul_i32 s14, s13, 0x104
	s_mul_i32 s15, s13, 0x110
	v_add_f32_e32 v6, v6, v7
	v_add_u32_e32 v125, s14, v59
	ds_write_b32 v125, v6
	v_cvt_pk_bf16_f32 v8, v140, v141
	v_cvt_pk_bf16_f32 v9, v142, v143
	v_add_u32_e32 v10, s15, v76
	s_mov_b64 exec, s[48:49]
	ds_write_b64 v10, v[8:9]
	s_mov_b64 exec, -1
	s_waitcnt vmcnt(12)
	v_mul_f32_e32 v11, v117, v145
	v_mul_f32_e32 v15, v119, v147
	v_fmac_f32_e32 v11, v116, v144
	v_fmac_f32_e32 v15, v118, v146
	s_add_i32 s13, s2, 3
	s_and_b32 s13, s13, 15
	s_mul_i32 s14, s13, 0x104
	s_mul_i32 s15, s13, 0x110
	v_add_f32_e32 v11, v11, v15
	v_add_u32_e32 v16, s14, v59
	ds_write_b32 v16, v11
	v_cvt_pk_bf16_f32 v12, v144, v145
	v_cvt_pk_bf16_f32 v13, v146, v147
	v_add_u32_e32 v14, s15, v76
	s_mov_b64 exec, s[48:49]
	ds_write_b64 v14, v[12:13]
	s_mov_b64 exec, -1
	s_waitcnt vmcnt(11)
	v_mul_f32_e32 v6, v117, v149
	v_mul_f32_e32 v7, v119, v151
	v_fmac_f32_e32 v6, v116, v148
	v_fmac_f32_e32 v7, v118, v150
	s_add_i32 s13, s2, 4
	s_and_b32 s13, s13, 15
	s_mul_i32 s14, s13, 0x104
	s_mul_i32 s15, s13, 0x110
	v_add_f32_e32 v6, v6, v7
	v_add_u32_e32 v125, s14, v59
	ds_write_b32 v125, v6
	v_cvt_pk_bf16_f32 v8, v148, v149
	v_cvt_pk_bf16_f32 v9, v150, v151
	v_add_u32_e32 v10, s15, v76
	s_mov_b64 exec, s[48:49]
	ds_write_b64 v10, v[8:9]
	s_mov_b64 exec, -1
	s_waitcnt vmcnt(10)
	v_mul_f32_e32 v11, v117, v153
	v_mul_f32_e32 v15, v119, v155
	v_fmac_f32_e32 v11, v116, v152
	v_fmac_f32_e32 v15, v118, v154
	s_add_i32 s13, s2, 5
	s_and_b32 s13, s13, 15
	s_mul_i32 s14, s13, 0x104
	s_mul_i32 s15, s13, 0x110
	v_add_f32_e32 v11, v11, v15
	v_add_u32_e32 v16, s14, v59
	ds_write_b32 v16, v11
	v_cvt_pk_bf16_f32 v12, v152, v153
	v_cvt_pk_bf16_f32 v13, v154, v155
	v_add_u32_e32 v14, s15, v76
	s_mov_b64 exec, s[48:49]
	ds_write_b64 v14, v[12:13]
	s_mov_b64 exec, -1
	s_waitcnt vmcnt(9)
	v_mul_f32_e32 v6, v117, v157
	v_mul_f32_e32 v7, v119, v159
	v_fmac_f32_e32 v6, v116, v156
	v_fmac_f32_e32 v7, v118, v158
	s_add_i32 s13, s2, 6
	s_and_b32 s13, s13, 15
	s_mul_i32 s14, s13, 0x104
	s_mul_i32 s15, s13, 0x110
	v_add_f32_e32 v6, v6, v7
	v_add_u32_e32 v125, s14, v59
	ds_write_b32 v125, v6
	v_cvt_pk_bf16_f32 v8, v156, v157
	v_cvt_pk_bf16_f32 v9, v158, v159
	v_add_u32_e32 v10, s15, v76
	s_mov_b64 exec, s[48:49]
	ds_write_b64 v10, v[8:9]
	s_mov_b64 exec, -1
	s_waitcnt vmcnt(8)
	v_mul_f32_e32 v11, v117, v161
	v_mul_f32_e32 v15, v119, v163
	v_fmac_f32_e32 v11, v116, v160
	v_fmac_f32_e32 v15, v118, v162
	s_add_i32 s13, s2, 7
	s_and_b32 s13, s13, 15
	s_mul_i32 s14, s13, 0x104
	s_mul_i32 s15, s13, 0x110
	v_add_f32_e32 v11, v11, v15
	v_add_u32_e32 v16, s14, v59
	ds_write_b32 v16, v11
	v_cvt_pk_bf16_f32 v12, v160, v161
	v_cvt_pk_bf16_f32 v13, v162, v163
	v_add_u32_e32 v14, s15, v76
	s_mov_b64 exec, s[48:49]
	ds_write_b64 v14, v[12:13]
	s_mov_b64 exec, -1
	s_waitcnt vmcnt(7)
	v_mul_f32_e32 v6, v117, v165
	v_mul_f32_e32 v7, v119, v167
	v_fmac_f32_e32 v6, v116, v164
	v_fmac_f32_e32 v7, v118, v166
	s_add_i32 s13, s2, 8
	s_and_b32 s13, s13, 15
	s_mul_i32 s14, s13, 0x104
	s_mul_i32 s15, s13, 0x110
	v_add_f32_e32 v6, v6, v7
	v_add_u32_e32 v125, s14, v59
	ds_write_b32 v125, v6
	v_cvt_pk_bf16_f32 v8, v164, v165
	v_cvt_pk_bf16_f32 v9, v166, v167
	v_add_u32_e32 v10, s15, v76
	s_mov_b64 exec, s[48:49]
	ds_write_b64 v10, v[8:9]
	s_mov_b64 exec, -1
	s_waitcnt vmcnt(6)
	v_mul_f32_e32 v11, v117, v169
	v_mul_f32_e32 v15, v119, v171
	v_fmac_f32_e32 v11, v116, v168
	v_fmac_f32_e32 v15, v118, v170
	s_add_i32 s13, s2, 9
	s_and_b32 s13, s13, 15
	s_mul_i32 s14, s13, 0x104
	s_mul_i32 s15, s13, 0x110
	v_add_f32_e32 v11, v11, v15
	v_add_u32_e32 v16, s14, v59
	ds_write_b32 v16, v11
	v_cvt_pk_bf16_f32 v12, v168, v169
	v_cvt_pk_bf16_f32 v13, v170, v171
	v_add_u32_e32 v14, s15, v76
	s_mov_b64 exec, s[48:49]
	ds_write_b64 v14, v[12:13]
	s_mov_b64 exec, -1
	s_waitcnt vmcnt(5)
	v_mul_f32_e32 v6, v117, v173
	v_mul_f32_e32 v7, v119, v175
	v_fmac_f32_e32 v6, v116, v172
	v_fmac_f32_e32 v7, v118, v174
	s_add_i32 s13, s2, 10
	s_and_b32 s13, s13, 15
	s_mul_i32 s14, s13, 0x104
	s_mul_i32 s15, s13, 0x110
	v_add_f32_e32 v6, v6, v7
	v_add_u32_e32 v125, s14, v59
	ds_write_b32 v125, v6
	v_cvt_pk_bf16_f32 v8, v172, v173
	v_cvt_pk_bf16_f32 v9, v174, v175
	v_add_u32_e32 v10, s15, v76
	s_mov_b64 exec, s[48:49]
	ds_write_b64 v10, v[8:9]
	s_mov_b64 exec, -1
	s_waitcnt vmcnt(4)
	v_mul_f32_e32 v11, v117, v177
	v_mul_f32_e32 v15, v119, v179
	v_fmac_f32_e32 v11, v116, v176
	v_fmac_f32_e32 v15, v118, v178
	s_add_i32 s13, s2, 11
	s_and_b32 s13, s13, 15
	s_mul_i32 s14, s13, 0x104
	s_mul_i32 s15, s13, 0x110
	v_add_f32_e32 v11, v11, v15
	v_add_u32_e32 v16, s14, v59
	ds_write_b32 v16, v11
	v_cvt_pk_bf16_f32 v12, v176, v177
	v_cvt_pk_bf16_f32 v13, v178, v179
	v_add_u32_e32 v14, s15, v76
	s_mov_b64 exec, s[48:49]
	ds_write_b64 v14, v[12:13]
	s_mov_b64 exec, -1
	s_waitcnt vmcnt(3)
	v_mul_f32_e32 v6, v117, v181
	v_mul_f32_e32 v7, v119, v183
	v_fmac_f32_e32 v6, v116, v180
	v_fmac_f32_e32 v7, v118, v182
	s_add_i32 s13, s2, 12
	s_and_b32 s13, s13, 15
	s_mul_i32 s14, s13, 0x104
	s_mul_i32 s15, s13, 0x110
	v_add_f32_e32 v6, v6, v7
	v_add_u32_e32 v125, s14, v59
	ds_write_b32 v125, v6
	v_cvt_pk_bf16_f32 v8, v180, v181
	v_cvt_pk_bf16_f32 v9, v182, v183
	v_add_u32_e32 v10, s15, v76
	s_mov_b64 exec, s[48:49]
	ds_write_b64 v10, v[8:9]
	s_mov_b64 exec, -1
	s_waitcnt vmcnt(2)
	v_mul_f32_e32 v11, v117, v185
	v_mul_f32_e32 v15, v119, v187
	v_fmac_f32_e32 v11, v116, v184
	v_fmac_f32_e32 v15, v118, v186
	s_add_i32 s13, s2, 13
	s_and_b32 s13, s13, 15
	s_mul_i32 s14, s13, 0x104
	s_mul_i32 s15, s13, 0x110
	v_add_f32_e32 v11, v11, v15
	v_add_u32_e32 v16, s14, v59
	ds_write_b32 v16, v11
	v_cvt_pk_bf16_f32 v12, v184, v185
	v_cvt_pk_bf16_f32 v13, v186, v187
	v_add_u32_e32 v14, s15, v76
	s_mov_b64 exec, s[48:49]
	ds_write_b64 v14, v[12:13]
	s_mov_b64 exec, -1
	s_waitcnt vmcnt(1)
	v_mul_f32_e32 v6, v117, v189
	v_mul_f32_e32 v7, v119, v191
	v_fmac_f32_e32 v6, v116, v188
	v_fmac_f32_e32 v7, v118, v190
	s_add_i32 s13, s2, 14
	s_and_b32 s13, s13, 15
	s_mul_i32 s14, s13, 0x104
	s_mul_i32 s15, s13, 0x110
	v_add_f32_e32 v6, v6, v7
	v_add_u32_e32 v125, s14, v59
	ds_write_b32 v125, v6
	v_cvt_pk_bf16_f32 v8, v188, v189
	v_cvt_pk_bf16_f32 v9, v190, v191
	v_add_u32_e32 v10, s15, v76
	s_mov_b64 exec, s[48:49]
	ds_write_b64 v10, v[8:9]
	s_mov_b64 exec, -1
	s_waitcnt vmcnt(0)
	v_mul_f32_e32 v11, v117, v193
	v_mul_f32_e32 v15, v119, v195
	v_fmac_f32_e32 v11, v116, v192
	v_fmac_f32_e32 v15, v118, v194
	s_add_i32 s13, s2, 15
	s_and_b32 s13, s13, 15
	s_mul_i32 s14, s13, 0x104
	s_mul_i32 s15, s13, 0x110
	v_add_f32_e32 v11, v11, v15
	v_add_u32_e32 v16, s14, v59
	ds_write_b32 v16, v11
	v_cvt_pk_bf16_f32 v12, v192, v193
	v_cvt_pk_bf16_f32 v13, v194, v195
	v_add_u32_e32 v14, s15, v76
	s_mov_b64 exec, s[48:49]
	ds_write_b64 v14, v[12:13]
	s_mov_b64 exec, -1
	s_waitcnt lgkmcnt(0)
	ds_read2_b32 v[60:61], v77 offset0:0 offset1:1
	ds_read2_b32 v[62:63], v77 offset0:2 offset1:3
	ds_read2_b32 v[64:65], v77 offset0:4 offset1:5
	ds_read2_b32 v[66:67], v77 offset0:6 offset1:7
	ds_read2_b32 v[68:69], v77 offset0:8 offset1:9
	ds_read2_b32 v[70:71], v77 offset0:10 offset1:11
	ds_read2_b32 v[72:73], v77 offset0:12 offset1:13
	ds_read2_b32 v[74:75], v77 offset0:14 offset1:15
	s_waitcnt lgkmcnt(0)
	v_add_f32_e32 v78, 0, v60
	v_add_f32_e32 v78, v78, v61
	v_add_f32_e32 v78, v78, v62
	v_add_f32_e32 v78, v78, v63
	v_add_f32_e32 v78, v78, v64
	v_add_f32_e32 v78, v78, v65
	v_add_f32_e32 v78, v78, v66
	v_add_f32_e32 v78, v78, v67
	v_add_f32_e32 v78, v78, v68
	v_add_f32_e32 v78, v78, v69
	v_add_f32_e32 v78, v78, v70
	v_add_f32_e32 v78, v78, v71
	v_add_f32_e32 v78, v78, v72
	v_add_f32_e32 v78, v78, v73
	v_add_f32_e32 v78, v78, v74
	v_add_f32_e32 v78, v78, v75
	s_nop 1
	v_add_f32_dpp v78, v78, v78 quad_perm:[1,0,3,2] row_mask:0xf bank_mask:0xf bound_ctrl:1
	s_nop 1
	v_add_f32_dpp v78, v78, v78 quad_perm:[2,3,0,1] row_mask:0xf bank_mask:0xf bound_ctrl:1
	v_lshlrev_b32_e32 v79, 4, v1
	ds_bpermute_b32 v78, v79, v78
	s_waitcnt lgkmcnt(0)
	s_barrier
	ds_read_b128 v[28:31], v53
	ds_read_b128 v[60:63], v56
	ds_read_b128 v[32:35], v53 offset:64
	ds_read_b128 v[64:67], v56 offset:64
	ds_read_b128 v[36:39], v53 offset:128
	ds_read_b128 v[68:71], v56 offset:128
	ds_read_b128 v[40:43], v53 offset:192
	ds_read_b128 v[72:75], v56 offset:192
	s_waitcnt lgkmcnt(6)
	v_mfma_f32_16x16x32_bf16 v[18:21], v[28:31], v[60:63], 0
	s_waitcnt lgkmcnt(4)
	v_mfma_f32_16x16x32_bf16 v[18:21], v[32:35], v[64:67], v[18:21]
	s_waitcnt lgkmcnt(2)
	v_mfma_f32_16x16x32_bf16 v[18:21], v[36:39], v[68:71], v[18:21]
	s_waitcnt lgkmcnt(0)
	v_mfma_f32_16x16x32_bf16 v[18:21], v[40:43], v[72:75], v[18:21]
	s_nop 7
	v_mul_f32_e32 v18, s44, v18
	v_mul_f32_e32 v19, s44, v19
	v_mul_f32_e32 v20, s44, v20
	v_mul_f32_e32 v21, s44, v21
	v_cvt_pk_bf16_f32 v18, v18, v18
	v_cvt_pk_bf16_f32 v19, v19, v19
	v_cvt_pk_bf16_f32 v20, v20, v20
	v_cvt_pk_bf16_f32 v21, v21, v21
	ds_write_b16 v55, v18
	ds_write_b16 v55, v19 offset:272
	ds_write_b16 v55, v20 offset:544
	ds_write_b16 v55, v21 offset:816
	s_waitcnt lgkmcnt(0)
	s_barrier
	ds_read_b128 v[28:31], v54
	ds_read_b128 v[60:63], v57
	ds_read_b128 v[32:35], v54 offset:64
	ds_read_b128 v[64:67], v57 offset:64
	ds_read_b128 v[36:39], v54 offset:128
	ds_read_b128 v[68:71], v57 offset:128
	ds_read_b128 v[40:43], v54 offset:192
	ds_read_b128 v[72:75], v57 offset:192
	s_waitcnt lgkmcnt(6)
	v_mfma_f32_16x16x32_bf16 v[18:21], v[28:31], v[60:63], 0
	s_waitcnt lgkmcnt(4)
	v_mfma_f32_16x16x32_bf16 v[18:21], v[32:35], v[64:67], v[18:21]
	s_waitcnt lgkmcnt(2)
	v_mfma_f32_16x16x32_bf16 v[18:21], v[36:39], v[68:71], v[18:21]
	s_waitcnt lgkmcnt(0)
	v_mfma_f32_16x16x32_bf16 v[18:21], v[40:43], v[72:75], v[18:21]
	s_nop 2
	v_mov_b32_e32 v28, v78
	s_load_dwordx2 s[4:5], s[0:1], 0x70
	v_lshl_or_b32 v30, v24, 2, s3
	v_ashrrev_i32_e32 v31, 31, v30
	v_mov_b32_e32 v107, 0
	s_waitcnt lgkmcnt(0)
	v_add_f32_e32 v34, v130, v28
	v_add_f32_e32 v35, v34, v18
	v_add_f32_e32 v28, v35, v35
	v_mul_f32_e32 v28, 0x3fb8aa3b, v28
	v_exp_f32_e32 v32, v28
	v_lshlrev_b64 v[28:29], 9, v[30:31]
	s_mov_b32 s8, 0x19200
	v_add3_u32 v37, v27, v25, s8
	v_add_f32_e32 v31, 1.0, v32
	v_rcp_f32_e32 v31, v31
	v_lshl_add_u64 v[32:33], s[4:5], 0, v[106:107]
	v_lshl_add_u64 v[28:29], v[32:33], 0, v[28:29]
	global_store_dword v[28:29], v35, off sc1
	v_fma_f32 v35, v31, -2.0, 1.0
	v_fma_f32 v28, -v35, v35, 1.0
	v_mul_f32_e32 v28, v129, v28
	v_add_f32_e32 v31, v34, v19
	v_cvt_pk_bf16_f32 v29, v28, s0
	v_mul_f32_e64 v27, v35, -v28
	v_add_f32_e32 v28, v31, v31
	v_mul_f32_e32 v28, 0x3fb8aa3b, v28
	v_exp_f32_e32 v38, v28
	v_cvt_pk_bf16_f32 v27, v27, s0
	ds_write_b16 v37, v27 offset:4352
	v_or_b32_e32 v28, 1, v30
	v_add_f32_e32 v27, 1.0, v38
	v_rcp_f32_e32 v27, v27
	ds_write_b16 v37, v29
	v_ashrrev_i32_e32 v29, 31, v28
	v_lshlrev_b64 v[28:29], 9, v[28:29]
	v_lshl_add_u64 v[28:29], v[32:33], 0, v[28:29]
	v_fma_f32 v27, v27, -2.0, 1.0
	global_store_dword v[28:29], v31, off sc1
	v_fma_f32 v28, -v27, v27, 1.0
	v_mul_f32_e32 v28, v129, v28
	v_cvt_pk_bf16_f32 v29, v28, s0
	v_add_f32_e32 v31, v34, v20
	ds_write_b16 v37, v29 offset:272
	v_add_f32_e32 v29, v31, v31
	v_mul_f32_e32 v29, 0x3fb8aa3b, v29
	v_exp_f32_e32 v38, v29
	v_mul_f32_e64 v28, v27, -v28
	v_cvt_pk_bf16_f32 v28, v28, s0
	ds_write_b16 v37, v28 offset:4624
	v_add_f32_e32 v38, 1.0, v38
	v_or_b32_e32 v28, 2, v30
	v_rcp_f32_e32 v38, v38
	v_ashrrev_i32_e32 v29, 31, v28
	v_lshlrev_b64 v[28:29], 9, v[28:29]
	v_lshl_add_u64 v[28:29], v[32:33], 0, v[28:29]
	global_store_dword v[28:29], v31, off sc1
	v_fma_f32 v28, v38, -2.0, 1.0
	v_fma_f32 v29, -v28, v28, 1.0
	v_mul_f32_e32 v29, v129, v29
	v_cvt_pk_bf16_f32 v31, v29, s0
	v_add_f32_e32 v34, v34, v21
	ds_write_b16 v37, v31 offset:544
	v_add_f32_e32 v31, v34, v34
	v_mul_f32_e32 v31, 0x3fb8aa3b, v31
	v_exp_f32_e32 v38, v31
	v_mul_f32_e64 v29, v28, -v29
	v_cvt_pk_bf16_f32 v29, v29, s0
	ds_write_b16 v37, v29 offset:4896
	v_add_f32_e32 v29, 1.0, v38
	v_rcp_f32_e32 v29, v29
	v_or_b32_e32 v30, 3, v30
	v_ashrrev_i32_e32 v31, 31, v30
	v_lshlrev_b64 v[30:31], 9, v[30:31]
	v_lshl_add_u64 v[30:31], v[32:33], 0, v[30:31]
	v_fma_f32 v29, v29, -2.0, 1.0
	global_store_dword v[30:31], v34, off sc1
	v_fma_f32 v30, -v29, v29, 1.0
	v_mul_f32_e32 v30, v129, v30
	v_cvt_pk_bf16_f32 v31, v30, s0
	v_mul_f32_e64 v30, v29, -v30
	v_cvt_pk_bf16_f32 v30, v30, s0
	ds_write_b16 v37, v30 offset:5168
	v_mov_b32_e32 v30, 0x1d800
	v_mul_f32_e32 v36, v129, v35
	v_lshl_or_b32 v32, v128, 6, v30
	v_mov_b32_e32 v30, v107
	ds_write_b16 v37, v31 offset:816
	v_mov_b32_e32 v31, 0
	v_mov_b32_dpp v30, v36 quad_perm:[1,0,3,2] row_mask:0xf bank_mask:0xf
	v_fmac_f32_e32 v30, v129, v35
	v_cmp_eq_u32_e32 vcc, 0, v1
	v_add_u32_e32 v26, v32, v26
	v_add_f32_dpp v30, v30, v30 quad_perm:[2,3,0,1] row_mask:0xf bank_mask:0xf bound_ctrl:1
	s_nop 1
	v_add_f32_dpp v30, v30, v30 row_half_mirror row_mask:0xf bank_mask:0xf bound_ctrl:1
	s_nop 1
	v_mov_b32_dpp v31, v30 row_mirror row_mask:0xf bank_mask:0xf
	s_and_saveexec_b64 s[4:5], vcc
	v_add_f32_e32 v30, v30, v31
	ds_write_b32 v26, v30
	s_or_b64 exec, exec, s[4:5]
	v_mul_f32_e32 v30, v129, v27
	v_mov_b32_e32 v31, 0
	s_nop 1
	v_mov_b32_dpp v31, v30 quad_perm:[1,0,3,2] row_mask:0xf bank_mask:0xf
	v_fmac_f32_e32 v31, v129, v27
	s_nop 1
	v_add_f32_dpp v27, v31, v31 quad_perm:[2,3,0,1] row_mask:0xf bank_mask:0xf bound_ctrl:1
	s_nop 1
	v_add_f32_dpp v27, v27, v27 row_half_mirror row_mask:0xf bank_mask:0xf bound_ctrl:1
	s_nop 1
	v_mov_b32_dpp v107, v27 row_mirror row_mask:0xf bank_mask:0xf
	s_and_saveexec_b64 s[4:5], vcc
	v_add_f32_e32 v27, v27, v107
	ds_write_b32 v26, v27 offset:4
	s_or_b64 exec, exec, s[4:5]
	v_mul_f32_e32 v30, v129, v28
	v_mov_b32_e32 v31, 0
	v_mov_b32_e32 v27, 0
	s_nop 0
	v_mov_b32_dpp v31, v30 quad_perm:[1,0,3,2] row_mask:0xf bank_mask:0xf
	v_fmac_f32_e32 v31, v129, v28
	v_mov_b32_e32 v30, 0
	s_nop 0
	v_add_f32_dpp v28, v31, v31 quad_perm:[2,3,0,1] row_mask:0xf bank_mask:0xf bound_ctrl:1
	s_nop 1
	v_add_f32_dpp v28, v28, v28 row_half_mirror row_mask:0xf bank_mask:0xf bound_ctrl:1
	s_nop 1
	v_mov_b32_dpp v30, v28 row_mirror row_mask:0xf bank_mask:0xf
	s_and_saveexec_b64 s[4:5], vcc
	v_add_f32_e32 v28, v28, v30
	ds_write_b32 v26, v28 offset:8
	s_or_b64 exec, exec, s[4:5]
	v_mul_f32_e32 v28, v129, v29
	v_mov_b32_e32 v30, 0
	s_nop 1
	v_mov_b32_dpp v30, v28 quad_perm:[1,0,3,2] row_mask:0xf bank_mask:0xf
	v_fmac_f32_e32 v30, v129, v29
	s_nop 1
	v_add_f32_dpp v28, v30, v30 quad_perm:[2,3,0,1] row_mask:0xf bank_mask:0xf bound_ctrl:1
	s_nop 1
	v_add_f32_dpp v28, v28, v28 row_half_mirror row_mask:0xf bank_mask:0xf bound_ctrl:1
	s_nop 1
	v_mov_b32_dpp v27, v28 row_mirror row_mask:0xf bank_mask:0xf
	s_and_saveexec_b64 s[4:5], vcc
	v_add_f32_e32 v27, v28, v27
	ds_write_b32 v26, v27 offset:12
	s_or_b64 exec, exec, s[4:5]
	s_mov_b64 s[4:5], 0
	s_branch .LBB0_28
.Lp_q:
	v_lshrrev_b32_e32 v122, 5, v0
	v_lshlrev_b32_e32 v122, 10, v122
	v_and_b32_e32 v125, 31, v0
	v_lshl_add_u32 v122, v125, 4, v122
	s_and_b32 s13, s2, 7
	s_lshl_b32 s14, s13, 14
	v_add_u32_e32 v125, s14, v122
	global_load_dwordx4 v[132:135], v125, s[28:29]
	s_add_i32 s13, s2, 1
	s_and_b32 s13, s13, 7
	s_lshl_b32 s14, s13, 14
	v_add_u32_e32 v125, s14, v122
	global_load_dwordx4 v[136:139], v125, s[28:29]
	s_add_i32 s13, s2, 2
	s_and_b32 s13, s13, 7
	s_lshl_b32 s14, s13, 14
	v_add_u32_e32 v125, s14, v122
	global_load_dwordx4 v[140:143], v125, s[28:29]
	s_add_i32 s13, s2, 3
	s_and_b32 s13, s13, 7
	s_lshl_b32 s14, s13, 14
	v_add_u32_e32 v125, s14, v122
	global_load_dwordx4 v[144:147], v125, s[28:29]
	s_add_i32 s13, s2, 4
	s_and_b32 s13, s13, 7
	s_lshl_b32 s14, s13, 14
	v_add_u32_e32 v125, s14, v122
	global_load_dwordx4 v[148:151], v125, s[28:29]
	s_add_i32 s13, s2, 5
	s_and_b32 s13, s13, 7
	s_lshl_b32 s14, s13, 14
	v_add_u32_e32 v125, s14, v122
	global_load_dwordx4 v[152:155], v125, s[28:29]
	s_add_i32 s13, s2, 6
	s_and_b32 s13, s13, 7
	s_lshl_b32 s14, s13, 14
	v_add_u32_e32 v125, s14, v122
	global_load_dwordx4 v[156:159], v125, s[28:29]
	s_add_i32 s13, s2, 7
	s_and_b32 s13, s13, 7
	s_lshl_b32 s14, s13, 14
	v_add_u32_e32 v125, s14, v122
	global_load_dwordx4 v[160:163], v125, s[28:29]
	s_waitcnt vmcnt(18)
	v_cvt_pk_bf16_f32 v12, v2, v3
	v_cvt_pk_bf16_f32 v13, v4, v5
	ds_write_b64 v124, v[12:13]
	s_waitcnt vmcnt(17)
	v_cvt_pk_bf16_f32 v6, v80, v81
	v_cvt_pk_bf16_f32 v7, v82, v83
	s_and_b32 s13, s2, 7
	s_mul_i32 s14, s13, 0x1100
	v_add_u32_e32 v125, s14, v58
	ds_write_b64 v125, v[6:7]
	s_waitcnt vmcnt(16)
	v_cvt_pk_bf16_f32 v8, v84, v85
	v_cvt_pk_bf16_f32 v9, v86, v87
	s_add_i32 s13, s2, 1
	s_and_b32 s13, s13, 7
	s_mul_i32 s14, s13, 0x1100
	v_add_u32_e32 v10, s14, v58
	ds_write_b64 v10, v[8:9]
	s_waitcnt vmcnt(15)
	v_cvt_pk_bf16_f32 v6, v88, v89
	v_cvt_pk_bf16_f32 v7, v90, v91
	s_add_i32 s13, s2, 2
	s_and_b32 s13, s13, 7
	s_mul_i32 s14, s13, 0x1100
	v_add_u32_e32 v125, s14, v58
	ds_write_b64 v125, v[6:7]
	s_waitcnt vmcnt(14)
	v_cvt_pk_bf16_f32 v8, v92, v93
	v_cvt_pk_bf16_f32 v9, v94, v95
	s_add_i32 s13, s2, 3
	s_and_b32 s13, s13, 7
	s_mul_i32 s14, s13, 0x1100
	v_add_u32_e32 v10, s14, v58
	ds_write_b64 v10, v[8:9]
	s_waitcnt vmcnt(13)
	v_cvt_pk_bf16_f32 v6, v96, v97
	v_cvt_pk_bf16_f32 v7, v98, v99
	s_add_i32 s13, s2, 4
	s_and_b32 s13, s13, 7
	s_mul_i32 s14, s13, 0x1100
	v_add_u32_e32 v125, s14, v58
	ds_write_b64 v125, v[6:7]
	s_waitcnt vmcnt(12)
	v_cvt_pk_bf16_f32 v8, v100, v101
	v_cvt_pk_bf16_f32 v9, v102, v103
	s_add_i32 s13, s2, 5
	s_and_b32 s13, s13, 7
	s_mul_i32 s14, s13, 0x1100
	v_add_u32_e32 v10, s14, v58
	ds_write_b64 v10, v[8:9]
	s_waitcnt vmcnt(11)
	v_cvt_pk_bf16_f32 v6, v108, v109
	v_cvt_pk_bf16_f32 v7, v110, v111
	s_add_i32 s13, s2, 6
	s_and_b32 s13, s13, 7
	s_mul_i32 s14, s13, 0x1100
	v_add_u32_e32 v125, s14, v58
	ds_write_b64 v125, v[6:7]
	s_waitcnt vmcnt(10)
	v_cvt_pk_bf16_f32 v8, v112, v113
	v_cvt_pk_bf16_f32 v9, v114, v115
	s_add_i32 s13, s2, 7
	s_and_b32 s13, s13, 7
	s_mul_i32 s14, s13, 0x1100
	v_add_u32_e32 v10, s14, v58
	ds_write_b64 v10, v[8:9]
	s_waitcnt vmcnt(7)
	v_cvt_pk_bf16_f32 v6, v132, v133
	v_cvt_pk_bf16_f32 v7, v134, v135
	s_and_b32 s13, s2, 7
	s_mul_i32 s14, s13, 0x1100
	s_add_i32 s14, s14, 34816
	v_add_u32_e32 v125, s14, v58
	ds_write_b64 v125, v[6:7]
	s_waitcnt vmcnt(6)
	v_cvt_pk_bf16_f32 v8, v136, v137
	v_cvt_pk_bf16_f32 v9, v138, v139
	s_add_i32 s13, s2, 1
	s_and_b32 s13, s13, 7
	s_mul_i32 s14, s13, 0x1100
	s_add_i32 s14, s14, 34816
	v_add_u32_e32 v10, s14, v58
	ds_write_b64 v10, v[8:9]
	s_waitcnt vmcnt(5)
	v_cvt_pk_bf16_f32 v6, v140, v141
	v_cvt_pk_bf16_f32 v7, v142, v143
	s_add_i32 s13, s2, 2
	s_and_b32 s13, s13, 7
	s_mul_i32 s14, s13, 0x1100
	s_add_i32 s14, s14, 34816
	v_add_u32_e32 v125, s14, v58
	ds_write_b64 v125, v[6:7]
	s_waitcnt vmcnt(4)
	v_cvt_pk_bf16_f32 v8, v144, v145
	v_cvt_pk_bf16_f32 v9, v146, v147
	s_add_i32 s13, s2, 3
	s_and_b32 s13, s13, 7
	s_mul_i32 s14, s13, 0x1100
	s_add_i32 s14, s14, 34816
	v_add_u32_e32 v10, s14, v58
	ds_write_b64 v10, v[8:9]
	s_waitcnt vmcnt(3)
	v_cvt_pk_bf16_f32 v6, v148, v149
	v_cvt_pk_bf16_f32 v7, v150, v151
	s_add_i32 s13, s2, 4
	s_and_b32 s13, s13, 7
	s_mul_i32 s14, s13, 0x1100
	s_add_i32 s14, s14, 34816
	v_add_u32_e32 v125, s14, v58
	ds_write_b64 v125, v[6:7]
	s_waitcnt vmcnt(2)
	v_cvt_pk_bf16_f32 v8, v152, v153
	v_cvt_pk_bf16_f32 v9, v154, v155
	s_add_i32 s13, s2, 5
	s_and_b32 s13, s13, 7
	s_mul_i32 s14, s13, 0x1100
	s_add_i32 s14, s14, 34816
	v_add_u32_e32 v10, s14, v58
	ds_write_b64 v10, v[8:9]
	s_waitcnt vmcnt(1)
	v_cvt_pk_bf16_f32 v6, v156, v157
	v_cvt_pk_bf16_f32 v7, v158, v159
	s_add_i32 s13, s2, 6
	s_and_b32 s13, s13, 7
	s_mul_i32 s14, s13, 0x1100
	s_add_i32 s14, s14, 34816
	v_add_u32_e32 v125, s14, v58
	ds_write_b64 v125, v[6:7]
	s_waitcnt vmcnt(0)
	v_cvt_pk_bf16_f32 v8, v160, v161
	v_cvt_pk_bf16_f32 v9, v162, v163
	s_add_i32 s13, s2, 7
	s_and_b32 s13, s13, 7
	s_mul_i32 s14, s13, 0x1100
	s_add_i32 s14, s14, 34816
	v_add_u32_e32 v10, s14, v58
	ds_write_b64 v10, v[8:9]
	s_waitcnt lgkmcnt(0)
	s_barrier
	v_lshl_add_u32 v123, v128, 1, s12
	v_lshlrev_b32_e32 v123, 12, v123
	v_lshl_add_u32 v123, v126, 4, v123
	v_add_u32_e32 v125, 0x1000, v123
	global_load_dwordx4 v[2:5], v123, s[34:35] nt
	global_load_dwordx4 v[6:9], v123, s[34:35] offset:1024 nt
	global_load_dwordx4 v[10:13], v123, s[34:35] offset:2048 nt
	global_load_dwordx4 v[14:17], v123, s[34:35] offset:3072 nt
	global_load_dwordx4 v[132:135], v125, s[34:35] nt
	global_load_dwordx4 v[136:139], v125, s[34:35] offset:1024 nt
	global_load_dwordx4 v[140:143], v125, s[34:35] offset:2048 nt
	global_load_dwordx4 v[144:147], v125, s[34:35] offset:3072 nt
	ds_read_b128 v[28:31], v53
	ds_read_b128 v[60:63], v56
	ds_read_b128 v[32:35], v53 offset:64
	ds_read_b128 v[64:67], v56 offset:64
	ds_read_b128 v[36:39], v53 offset:128
	ds_read_b128 v[68:71], v56 offset:128
	ds_read_b128 v[40:43], v53 offset:192
	ds_read_b128 v[72:75], v56 offset:192
	s_waitcnt lgkmcnt(6)
	v_mfma_f32_16x16x32_bf16 v[18:21], v[28:31], v[60:63], 0
	s_waitcnt lgkmcnt(4)
	v_mfma_f32_16x16x32_bf16 v[18:21], v[32:35], v[64:67], v[18:21]
	s_waitcnt lgkmcnt(2)
	v_mfma_f32_16x16x32_bf16 v[18:21], v[36:39], v[68:71], v[18:21]
	s_waitcnt lgkmcnt(0)
	v_mfma_f32_16x16x32_bf16 v[18:21], v[40:43], v[72:75], v[18:21]
	s_nop 7
	v_mul_f32_e32 v18, s44, v18
	v_mul_f32_e32 v19, s44, v19
	v_mul_f32_e32 v20, s44, v20
	v_mul_f32_e32 v21, s44, v21
	v_cvt_pk_bf16_f32 v18, v18, v18
	v_cvt_pk_bf16_f32 v19, v19, v19
	v_cvt_pk_bf16_f32 v20, v20, v20
	v_cvt_pk_bf16_f32 v21, v21, v21
	ds_write_b16 v55, v18
	ds_write_b16 v55, v19 offset:272
	ds_write_b16 v55, v20 offset:544
	ds_write_b16 v55, v21 offset:816
	s_waitcnt lgkmcnt(0)
	s_barrier
	ds_read_b128 v[28:31], v54
	ds_read_b128 v[60:63], v57
	ds_read_b128 v[32:35], v54 offset:64
	ds_read_b128 v[64:67], v57 offset:64
	ds_read_b128 v[36:39], v54 offset:128
	ds_read_b128 v[68:71], v57 offset:128
	ds_read_b128 v[40:43], v54 offset:192
	ds_read_b128 v[72:75], v57 offset:192
	s_waitcnt lgkmcnt(6)
	v_mfma_f32_16x16x32_bf16 v[18:21], v[28:31], v[60:63], 0
	s_waitcnt lgkmcnt(4)
	v_mfma_f32_16x16x32_bf16 v[18:21], v[32:35], v[64:67], v[18:21]
	s_waitcnt lgkmcnt(2)
	v_mfma_f32_16x16x32_bf16 v[18:21], v[36:39], v[68:71], v[18:21]
	s_waitcnt lgkmcnt(0)
	v_mfma_f32_16x16x32_bf16 v[18:21], v[40:43], v[72:75], v[18:21]
	s_load_dwordx2 s[4:5], s[0:1], 0x68
	v_lshl_or_b32 v26, v24, 2, s12
	v_mov_b32_e32 v107, 0
	v_ashrrev_i32_e32 v27, 31, v26
	v_lshlrev_b64 v[28:29], 9, v[26:27]
	s_waitcnt lgkmcnt(0)
	v_lshl_add_u64 v[30:31], s[4:5], 0, v[106:107]
	v_lshl_add_u64 v[28:29], v[30:31], 0, v[28:29]
	v_mul_u32_u24_e32 v24, 0x440, v24
	s_mov_b32 s4, 0x19200
	global_store_dword v[28:29], v18, off sc1
	v_add3_u32 v28, v24, v25, s4
	v_mul_f32_e32 v24, v18, v18
	v_cvt_pk_bf16_f32 v27, v18, s0
	v_cvt_pk_bf16_f32 v24, v24, s0
	ds_write_b16 v28, v27
	ds_write_b16 v28, v24 offset:4352
	v_max3_f32 v27, |v18|, 0, |v19|
	v_or_b32_e32 v24, 1, v26
	v_cvt_pk_bf16_f32 v18, v19, s0
	v_ashrrev_i32_e32 v25, 31, v24
	ds_write_b16 v28, v18 offset:272
	v_mul_f32_e32 v18, v19, v19
	v_lshlrev_b64 v[24:25], 9, v[24:25]
	v_cvt_pk_bf16_f32 v18, v18, s0
	v_lshl_add_u64 v[24:25], v[30:31], 0, v[24:25]
	ds_write_b16 v28, v18 offset:4624
	v_or_b32_e32 v18, 2, v26
	global_store_dword v[24:25], v19, off sc1
	v_ashrrev_i32_e32 v19, 31, v18
	v_lshlrev_b64 v[18:19], 9, v[18:19]
	v_lshl_add_u64 v[18:19], v[30:31], 0, v[18:19]
	global_store_dword v[18:19], v20, off sc1
	v_cvt_pk_bf16_f32 v18, v20, s0
	ds_write_b16 v28, v18 offset:544
	v_mul_f32_e32 v18, v20, v20
	v_cvt_pk_bf16_f32 v18, v18, s0
	ds_write_b16 v28, v18 offset:4896
	v_or_b32_e32 v18, 3, v26
	v_ashrrev_i32_e32 v19, 31, v18
	v_lshlrev_b64 v[18:19], 9, v[18:19]
	v_lshl_add_u64 v[18:19], v[30:31], 0, v[18:19]
	global_store_dword v[18:19], v21, off sc1
	v_cvt_pk_bf16_f32 v18, v21, s0
	ds_write_b16 v28, v18 offset:816
	v_mul_f32_e32 v18, v21, v21
	v_cvt_pk_bf16_f32 v18, v18, s0
	v_max3_f32 v20, v27, |v20|, |v21|
	ds_write_b16 v28, v18 offset:5168
	v_mov_b32_e32 v18, v107
	v_mov_b32_e32 v19, v107
	v_cmp_eq_u32_e32 vcc, 0, v126
	v_mov_b32_dpp v18, v20 quad_perm:[1,0,3,2] row_mask:0xf bank_mask:0xf
	v_max_f32_e32 v18, v18, v18
	v_max_f32_e32 v18, v20, v18
	s_nop 1
	v_mov_b32_dpp v19, v18 quad_perm:[2,3,0,1] row_mask:0xf bank_mask:0xf
	v_max_f32_e32 v19, v19, v19
	v_max_f32_e32 v18, v18, v19
	v_mov_b32_e32 v19, v107
	s_nop 1
	v_mov_b32_dpp v19, v18 row_half_mirror row_mask:0xf bank_mask:0xf
	v_max_f32_e32 v19, v19, v19
	v_max_f32_e32 v18, v18, v19
	v_mov_b32_e32 v19, v107
	s_nop 1
	v_mov_b32_dpp v19, v18 row_mirror row_mask:0xf bank_mask:0xf
	v_max_f32_e32 v19, v19, v19
	v_max_f32_e32 v18, v18, v19
	s_nop 0
	v_readlane_b32 s8, v18, 0
	v_readlane_b32 s9, v18, 16
	v_readlane_b32 s10, v18, 32
	v_readlane_b32 s11, v18, 48
	v_and_b32_e32 v18, 0x7fffffff, v129
	s_nop 1
	v_add_f32_dpp v18, v18, |v129| quad_perm:[1,0,3,2] row_mask:0xf bank_mask:0xf bound_ctrl:1
	s_nop 1
	v_add_f32_dpp v18, v18, v18 quad_perm:[2,3,0,1] row_mask:0xf bank_mask:0xf bound_ctrl:1
	s_nop 1
	v_add_f32_dpp v18, v18, v18 row_half_mirror row_mask:0xf bank_mask:0xf bound_ctrl:1
	s_nop 1
	v_mov_b32_dpp v107, v18 row_mirror row_mask:0xf bank_mask:0xf
	s_and_saveexec_b64 s[4:5], vcc
	s_cbranch_execz .LBB0_27
	v_mov_b32_e32 v19, 0x1d800
	v_lshl_or_b32 v20, v128, 6, v19
	v_add_f32_e32 v19, v18, v107
	v_max_f32_e64 v18, s11, s11
	v_max_f32_e64 v21, s10, s10
	v_max_f32_e32 v18, v21, v18
	v_mov_b32_e32 v21, s9
	v_max3_f32 v18, s8, v21, v18
	ds_write_b64 v20, v[18:19]

.LBB0_40:
	s_cmpk_gt_i32 s2, 0x7f
	s_cbranch_scc1 .Lp_end
	s_waitcnt vmcnt(9)
	v_mov_b32_e32 v44, 0
	v_cmp_ne_u32_e64 s[46:47], 0, v17
	v_cmp_ne_u32_e64 s[48:49], 0, v16
	v_cmp_ne_u32_e64 s[50:51], 0, v15
	v_cmp_ne_u32_e64 s[52:53], 0, v14
	v_addc_co_u32_e64 v44, s[54:55], v44, v44, s[46:47]
	v_addc_co_u32_e64 v44, s[54:55], v44, v44, s[48:49]
	v_addc_co_u32_e64 v44, s[54:55], v44, v44, s[50:51]
	v_addc_co_u32_e64 v44, s[54:55], v44, v44, s[52:53]
	v_cmp_ne_u32_e64 s[46:47], 0, v13
	v_cmp_ne_u32_e64 s[48:49], 0, v12
	v_cmp_ne_u32_e64 s[50:51], 0, v11
	v_cmp_ne_u32_e64 s[52:53], 0, v10
	v_addc_co_u32_e64 v44, s[54:55], v44, v44, s[46:47]
	v_addc_co_u32_e64 v44, s[54:55], v44, v44, s[48:49]
	v_addc_co_u32_e64 v44, s[54:55], v44, v44, s[50:51]
	v_addc_co_u32_e64 v44, s[54:55], v44, v44, s[52:53]
	v_cmp_ne_u32_e64 s[46:47], 0, v9
	v_cmp_ne_u32_e64 s[48:49], 0, v8
	v_cmp_ne_u32_e64 s[50:51], 0, v7
	v_cmp_ne_u32_e64 s[52:53], 0, v6
	v_addc_co_u32_e64 v44, s[54:55], v44, v44, s[46:47]
	v_addc_co_u32_e64 v44, s[54:55], v44, v44, s[48:49]
	v_addc_co_u32_e64 v44, s[54:55], v44, v44, s[50:51]
	v_addc_co_u32_e64 v44, s[54:55], v44, v44, s[52:53]
	v_cmp_ne_u32_e64 s[46:47], 0, v5
	v_cmp_ne_u32_e64 s[48:49], 0, v4
	v_cmp_ne_u32_e64 s[50:51], 0, v3
	v_cmp_ne_u32_e64 s[52:53], 0, v2
	v_addc_co_u32_e64 v44, s[54:55], v44, v44, s[46:47]
	v_addc_co_u32_e64 v44, s[54:55], v44, v44, s[48:49]
	v_addc_co_u32_e64 v44, s[54:55], v44, v44, s[50:51]
	v_addc_co_u32_e64 v44, s[54:55], v44, v44, s[52:53]
	s_waitcnt vmcnt(5)
	v_mov_b32_e32 v45, 0
	v_cmp_ne_u32_e64 s[46:47], 0, v147
	v_cmp_ne_u32_e64 s[48:49], 0, v146
	v_cmp_ne_u32_e64 s[50:51], 0, v145
	v_cmp_ne_u32_e64 s[52:53], 0, v144
	v_addc_co_u32_e64 v45, s[54:55], v45, v45, s[46:47]
	v_addc_co_u32_e64 v45, s[54:55], v45, v45, s[48:49]
	v_addc_co_u32_e64 v45, s[54:55], v45, v45, s[50:51]
	v_addc_co_u32_e64 v45, s[54:55], v45, v45, s[52:53]
	v_cmp_ne_u32_e64 s[46:47], 0, v143
	v_cmp_ne_u32_e64 s[48:49], 0, v142
	v_cmp_ne_u32_e64 s[50:51], 0, v141
	v_cmp_ne_u32_e64 s[52:53], 0, v140
	v_addc_co_u32_e64 v45, s[54:55], v45, v45, s[46:47]
	v_addc_co_u32_e64 v45, s[54:55], v45, v45, s[48:49]
	v_addc_co_u32_e64 v45, s[54:55], v45, v45, s[50:51]
	v_addc_co_u32_e64 v45, s[54:55], v45, v45, s[52:53]
	v_cmp_ne_u32_e64 s[46:47], 0, v139
	v_cmp_ne_u32_e64 s[48:49], 0, v138
	v_cmp_ne_u32_e64 s[50:51], 0, v137
	v_cmp_ne_u32_e64 s[52:53], 0, v136
	v_addc_co_u32_e64 v45, s[54:55], v45, v45, s[46:47]
	v_addc_co_u32_e64 v45, s[54:55], v45, v45, s[48:49]
	v_addc_co_u32_e64 v45, s[54:55], v45, v45, s[50:51]
	v_addc_co_u32_e64 v45, s[54:55], v45, v45, s[52:53]
	v_cmp_ne_u32_e64 s[46:47], 0, v135
	v_cmp_ne_u32_e64 s[48:49], 0, v134
	v_cmp_ne_u32_e64 s[50:51], 0, v133
	v_cmp_ne_u32_e64 s[52:53], 0, v132
	v_addc_co_u32_e64 v45, s[54:55], v45, v45, s[46:47]
	v_addc_co_u32_e64 v45, s[54:55], v45, v45, s[48:49]
	v_addc_co_u32_e64 v45, s[54:55], v45, v45, s[50:51]
	v_addc_co_u32_e64 v45, s[54:55], v45, v45, s[52:53]
	s_lshl_b32 s13, s2, 4
	v_lshl_add_u32 v46, v128, 1, s13
	v_lshlrev_b32_e32 v46, 7, v46
	v_lshl_add_u32 v46, v126, 1, v46
	global_store_short v46, v44, s[36:37] sc1
	global_store_short v46, v45, s[36:37] offset:128 sc1
